# P10: cooperative L2 prefetch of the next unit's tiles issued at the end of SP2(0) of the peeled first K-iteration (counted waits keep it in flight)
# speedup vs baseline: 1.0090x; 1.0090x over previous
.LBB0_1441:
	s_and_b64 vcc, exec, s[0:1]
	s_cmp_eq_u32 s98, 0
	s_cbranch_scc1 .Lgk_first_p10
	v_mov_b32_e32 v175, v169
	v_mov_b32_e32 v173, v169
	s_mov_b32 s23, 0
	s_mov_b64 s[34:35], 0x100
	s_mov_b64 s[36:37], s[16:17]
	v_readfirstlane_b32 s70, v0
	s_lshr_b32 s70, s70, 6
	s_cmp_eq_u64 s[2:3], 0
	s_cselect_b32 s71, s65, s66
	s_lshl_b32 s71, s71, 17
	s_lshl_b32 s72, s28, 14
	s_add_u32 s71, s71, s72
	s_and_b32 s72, s70, 1
	s_lshl_b32 s72, s72, 13
	s_add_u32 s71, s71, s72
	s_add_u32 s74, s12, s71
	s_addc_u32 s75, s13, 0
	s_bfe_u32 s72, s80, 0x20006
	s_lshl_b32 s72, s72, 15
	s_sub_u32 s73, s70, 2
	s_lshl_b32 s78, s73, 13
	s_add_u32 s72, s72, s78
	s_add_u32 s76, s26, s72
	s_addc_u32 s77, s27, 0
	s_cmp_lt_u32 s73, 4
	s_cselect_b64 s[74:75], s[76:77], s[74:75]
	v_lshlrev_b32_e32 v250, 7, v206
	ds_read_b128 v[26:29], v191
	ds_read_b128 v[30:33], v191 offset:1024
	ds_read_b128 v[18:21], v191 offset:2048
	ds_read_b128 v[22:25], v191 offset:3072
	ds_read_b128 v[10:13], v192
	ds_read_b128 v[14:17], v192 offset:1024
	ds_read_b128 v[2:5], v192 offset:2048
	ds_read_b128 v[6:9], v192 offset:3072
	s_cmp_eq_u32 s54, s23
	s_cselect_b64 vcc, -1, 0
	s_add_i32 s23, s23, 2
	s_and_b64 s[38:39], vcc, exec
	s_cselect_b32 s38, 0, s34
	s_cselect_b32 s25, 0, s35
	s_add_u32 s38, s12, s38
	s_addc_u32 s39, s13, s25
	s_add_u32 s25, s30, s34
	s_addc_u32 s67, s31, s35
	s_and_b64 s[40:41], vcc, exec
	v_cndmask_b32_e32 v168, v197, v198, vcc
	v_cndmask_b32_e32 v202, v172, v200, vcc
	v_cndmask_b32_e32 v184, v170, v199, vcc
	s_cselect_b32 s41, s27, s67
	s_cselect_b32 s40, s26, s25
	s_mov_b32 m0, s55
	v_lshl_add_u64 v[186:187], s[36:37], 0, v[172:173]
	ds_read_b128 v[176:179], v193
	ds_read_b128 v[180:183], v193 offset:1024
	ds_read_b128 v[208:211], v193 offset:2048
	ds_read_b128 v[212:215], v193 offset:3072
	ds_read_b128 v[216:219], v193 offset:4096
	ds_read_b128 v[220:223], v193 offset:5120
	ds_read_b128 v[224:227], v193 offset:6144
	ds_read_b128 v[228:231], v193 offset:7168
	global_load_lds_dwordx4 v[186:187], off
	v_lshl_add_u64 v[186:187], s[36:37], 0, v[174:175]
	s_mov_b32 m0, s56
	s_nop 0
	global_load_lds_dwordx4 v[186:187], off
	s_waitcnt vmcnt(16)
	s_waitcnt lgkmcnt(0)
	s_barrier
	s_setprio 1
	s_waitcnt lgkmcnt(0)
	v_mfma_scale_f32_16x16x128_f8f6f4 v[158:161], v[26:33], v[176:183], 0, v188, v189 op_sel_hi:[0,0,0]
	v_mfma_scale_f32_16x16x128_f8f6f4 v[154:157], v[18:25], v[176:183], 0, v188, v189 op_sel_hi:[0,0,0]
	v_mfma_scale_f32_16x16x128_f8f6f4 v[142:145], v[26:33], v[208:215], 0, v188, v189 op_sel_hi:[0,0,0]
	v_mfma_scale_f32_16x16x128_f8f6f4 v[138:141], v[18:25], v[208:215], 0, v188, v189 op_sel_hi:[0,0,0]
	v_mfma_scale_f32_16x16x128_f8f6f4 v[126:129], v[26:33], v[216:223], 0, v188, v189 op_sel_hi:[0,0,0]
	v_mfma_scale_f32_16x16x128_f8f6f4 v[122:125], v[18:25], v[216:223], 0, v188, v189 op_sel_hi:[0,0,0]
	v_mfma_scale_f32_16x16x128_f8f6f4 v[110:113], v[26:33], v[224:231], 0, v188, v189 op_sel_hi:[0,0,0]
	v_mfma_scale_f32_16x16x128_f8f6f4 v[106:109], v[18:25], v[224:231], 0, v188, v189 op_sel_hi:[0,0,0]
	s_setprio 0
	s_setprio 1
	v_mfma_scale_f32_16x16x128_f8f6f4 v[150:153], v[10:17], v[176:183], 0, v188, v189 op_sel_hi:[0,0,0]
	v_mfma_scale_f32_16x16x128_f8f6f4 v[146:149], v[2:9], v[176:183], 0, v188, v189 op_sel_hi:[0,0,0]
	v_mfma_scale_f32_16x16x128_f8f6f4 v[134:137], v[10:17], v[208:215], 0, v188, v189 op_sel_hi:[0,0,0]
	v_mfma_scale_f32_16x16x128_f8f6f4 v[130:133], v[2:9], v[208:215], 0, v188, v189 op_sel_hi:[0,0,0]
	v_mfma_scale_f32_16x16x128_f8f6f4 v[118:121], v[10:17], v[216:223], 0, v188, v189 op_sel_hi:[0,0,0]
	v_mfma_scale_f32_16x16x128_f8f6f4 v[114:117], v[2:9], v[216:223], 0, v188, v189 op_sel_hi:[0,0,0]
	v_mfma_scale_f32_16x16x128_f8f6f4 v[102:105], v[10:17], v[224:231], 0, v188, v189 op_sel_hi:[0,0,0]
	v_mfma_scale_f32_16x16x128_f8f6f4 v[98:101], v[2:9], v[224:231], 0, v188, v189 op_sel_hi:[0,0,0]
	s_setprio 0
	s_barrier
	s_mov_b32 m0, s57
	v_lshl_add_u64 v[176:177], s[40:41], 0, v[166:167]
	v_lshl_add_u64 v[178:179], s[40:41], 0, v[164:165]
	s_add_u32 s40, s40, s10
	ds_read_b128 v[208:211], v193 offset:16384
	ds_read_b128 v[212:215], v193 offset:17408
	ds_read_b128 v[216:219], v193 offset:18432
	ds_read_b128 v[220:223], v193 offset:19456
	ds_read_b128 v[224:227], v193 offset:20480
	ds_read_b128 v[228:231], v193 offset:21504
	ds_read_b128 v[232:235], v193 offset:22528
	ds_read_b128 v[236:239], v193 offset:23552
	global_load_lds_dwordx4 v[176:177], off
	s_mov_b32 m0, s58
	s_addc_u32 s41, s41, s11
	global_load_lds_dwordx4 v[178:179], off
	v_lshl_add_u64 v[180:181], s[40:41], 0, v[166:167]
	s_mov_b32 m0, s59
	v_lshl_add_u64 v[182:183], s[40:41], 0, v[164:165]
	global_load_lds_dwordx4 v[180:181], off
	s_mov_b32 m0, s60
	v_mov_b32_e32 v185, v169
	global_load_lds_dwordx4 v[182:183], off
	s_mov_b32 m0, s29
	v_lshl_add_u64 v[186:187], s[38:39], 0, v[168:169]
	global_load_lds_dwordx4 v168, s[38:39]
	s_mov_b32 m0, s46
	s_nop 0
	global_load_lds_dwordx4 v184, s[38:39]
	global_load_dword v251, v250, s[74:75]
	s_waitcnt vmcnt(17)
	s_waitcnt lgkmcnt(0)
	v_lshl_add_u64 v[184:185], s[38:39], 0, v[184:185]
	s_barrier
	s_setprio 1
	s_waitcnt lgkmcnt(0)
	v_mfma_scale_f32_16x16x128_f8f6f4 v[94:97], v[26:33], v[208:215], 0, v188, v189 op_sel_hi:[0,0,0]
	v_mfma_scale_f32_16x16x128_f8f6f4 v[90:93], v[18:25], v[208:215], 0, v188, v189 op_sel_hi:[0,0,0]
	v_mfma_scale_f32_16x16x128_f8f6f4 v[78:81], v[26:33], v[216:223], 0, v188, v189 op_sel_hi:[0,0,0]
	v_mfma_scale_f32_16x16x128_f8f6f4 v[74:77], v[18:25], v[216:223], 0, v188, v189 op_sel_hi:[0,0,0]
	v_mfma_scale_f32_16x16x128_f8f6f4 v[62:65], v[26:33], v[224:231], 0, v188, v189 op_sel_hi:[0,0,0]
	v_mfma_scale_f32_16x16x128_f8f6f4 v[58:61], v[18:25], v[224:231], 0, v188, v189 op_sel_hi:[0,0,0]
	v_mfma_scale_f32_16x16x128_f8f6f4 v[46:49], v[26:33], v[232:239], 0, v188, v189 op_sel_hi:[0,0,0]
	v_mfma_scale_f32_16x16x128_f8f6f4 v[42:45], v[18:25], v[232:239], 0, v188, v189 op_sel_hi:[0,0,0]
	s_setprio 0
	s_setprio 1
	v_mfma_scale_f32_16x16x128_f8f6f4 v[86:89], v[10:17], v[208:215], 0, v188, v189 op_sel_hi:[0,0,0]
	v_mfma_scale_f32_16x16x128_f8f6f4 v[82:85], v[2:9], v[208:215], 0, v188, v189 op_sel_hi:[0,0,0]
	v_mfma_scale_f32_16x16x128_f8f6f4 v[70:73], v[10:17], v[216:223], 0, v188, v189 op_sel_hi:[0,0,0]
	v_mfma_scale_f32_16x16x128_f8f6f4 v[66:69], v[2:9], v[216:223], 0, v188, v189 op_sel_hi:[0,0,0]
	v_mfma_scale_f32_16x16x128_f8f6f4 v[54:57], v[10:17], v[224:231], 0, v188, v189 op_sel_hi:[0,0,0]
	v_mfma_scale_f32_16x16x128_f8f6f4 v[50:53], v[2:9], v[224:231], 0, v188, v189 op_sel_hi:[0,0,0]
	v_mfma_scale_f32_16x16x128_f8f6f4 v[38:41], v[10:17], v[232:239], 0, v188, v189 op_sel_hi:[0,0,0]
	v_mfma_scale_f32_16x16x128_f8f6f4 v[34:37], v[2:9], v[232:239], 0, v188, v189 op_sel_hi:[0,0,0]
	s_setprio 0
	s_barrier
	ds_read_b128 v[26:29], v194
	ds_read_b128 v[30:33], v194 offset:1024
	ds_read_b128 v[18:21], v194 offset:2048
	ds_read_b128 v[22:25], v194 offset:3072
	ds_read_b128 v[10:13], v195
	ds_read_b128 v[14:17], v195 offset:1024
	ds_read_b128 v[2:5], v195 offset:2048
	ds_read_b128 v[6:9], v195 offset:3072
	s_mov_b32 m0, s47
	ds_read_b128 v[208:211], v193 offset:32768
	ds_read_b128 v[212:215], v193 offset:33792
	ds_read_b128 v[216:219], v193 offset:34816
	ds_read_b128 v[220:223], v193 offset:35840
	ds_read_b128 v[224:227], v193 offset:36864
	ds_read_b128 v[228:231], v193 offset:37888
	ds_read_b128 v[232:235], v193 offset:38912
	ds_read_b128 v[236:239], v193 offset:39936
	v_cndmask_b32_e32 v168, v174, v201, vcc
	global_load_lds_dwordx4 v202, s[38:39]
	s_mov_b32 m0, s48
	s_nop 0
	global_load_lds_dwordx4 v168, s[38:39]
	s_waitcnt vmcnt(9)
	s_waitcnt lgkmcnt(0)
	s_barrier
	s_setprio 1
	s_waitcnt lgkmcnt(0)
	v_mfma_scale_f32_16x16x128_f8f6f4 v[158:161], v[26:33], v[208:215], v[158:161], v188, v189 op_sel_hi:[0,0,0]
	v_mfma_scale_f32_16x16x128_f8f6f4 v[154:157], v[18:25], v[208:215], v[154:157], v188, v189 op_sel_hi:[0,0,0]
	v_mfma_scale_f32_16x16x128_f8f6f4 v[142:145], v[26:33], v[216:223], v[142:145], v188, v189 op_sel_hi:[0,0,0]
	v_mfma_scale_f32_16x16x128_f8f6f4 v[138:141], v[18:25], v[216:223], v[138:141], v188, v189 op_sel_hi:[0,0,0]
	v_mfma_scale_f32_16x16x128_f8f6f4 v[126:129], v[26:33], v[224:231], v[126:129], v188, v189 op_sel_hi:[0,0,0]
	v_mfma_scale_f32_16x16x128_f8f6f4 v[122:125], v[18:25], v[224:231], v[122:125], v188, v189 op_sel_hi:[0,0,0]
	v_mfma_scale_f32_16x16x128_f8f6f4 v[110:113], v[26:33], v[232:239], v[110:113], v188, v189 op_sel_hi:[0,0,0]
	v_mfma_scale_f32_16x16x128_f8f6f4 v[106:109], v[18:25], v[232:239], v[106:109], v188, v189 op_sel_hi:[0,0,0]
	s_setprio 0
	s_setprio 1
	v_mfma_scale_f32_16x16x128_f8f6f4 v[150:153], v[10:17], v[208:215], v[150:153], v188, v189 op_sel_hi:[0,0,0]
	v_mfma_scale_f32_16x16x128_f8f6f4 v[146:149], v[2:9], v[208:215], v[146:149], v188, v189 op_sel_hi:[0,0,0]
	v_mfma_scale_f32_16x16x128_f8f6f4 v[134:137], v[10:17], v[216:223], v[134:137], v188, v189 op_sel_hi:[0,0,0]
	v_mfma_scale_f32_16x16x128_f8f6f4 v[130:133], v[2:9], v[216:223], v[130:133], v188, v189 op_sel_hi:[0,0,0]
	v_mfma_scale_f32_16x16x128_f8f6f4 v[118:121], v[10:17], v[224:231], v[118:121], v188, v189 op_sel_hi:[0,0,0]
	v_mfma_scale_f32_16x16x128_f8f6f4 v[114:117], v[2:9], v[224:231], v[114:117], v188, v189 op_sel_hi:[0,0,0]
	v_mfma_scale_f32_16x16x128_f8f6f4 v[102:105], v[10:17], v[232:239], v[102:105], v188, v189 op_sel_hi:[0,0,0]
	v_mfma_scale_f32_16x16x128_f8f6f4 v[98:101], v[2:9], v[232:239], v[98:101], v188, v189 op_sel_hi:[0,0,0]
	s_setprio 0
	s_barrier
	s_mov_b32 m0, s61
	v_lshl_add_u64 v[176:177], v[176:177], 0, s[18:19]
	ds_read_b128 v[208:211], v193 offset:49152
	ds_read_b128 v[212:215], v193 offset:50176
	ds_read_b128 v[216:219], v193 offset:51200
	ds_read_b128 v[220:223], v193 offset:52224
	ds_read_b128 v[224:227], v193 offset:53248
	ds_read_b128 v[228:231], v193 offset:54272
	ds_read_b128 v[232:235], v193 offset:55296
	ds_read_b128 v[236:239], v193 offset:56320
	global_load_lds_dwordx4 v[176:177], off
	v_lshl_add_u64 v[176:177], v[178:179], 0, s[18:19]
	s_mov_b32 m0, s62
	s_nop 0
	global_load_lds_dwordx4 v[176:177], off
	v_lshl_add_u64 v[176:177], v[180:181], 0, s[18:19]
	s_mov_b32 m0, s63
	s_nop 0
	global_load_lds_dwordx4 v[176:177], off
	v_lshl_add_u64 v[176:177], v[182:183], 0, s[18:19]
	s_add_i32 m0, s63, 0x2000
	s_nop 0
	global_load_lds_dwordx4 v[176:177], off
	v_lshl_add_u64 v[176:177], v[186:187], 0, s[18:19]
	s_mov_b32 m0, s50
	s_nop 0
	global_load_lds_dwordx4 v[176:177], off
	v_lshl_add_u64 v[176:177], v[184:185], 0, s[18:19]
	s_mov_b32 m0, s51
	s_nop 0
	global_load_lds_dwordx4 v[176:177], off
	s_waitcnt vmcnt(9)
	s_waitcnt lgkmcnt(0)
	s_barrier
	s_setprio 1
	s_waitcnt lgkmcnt(0)
	v_mfma_scale_f32_16x16x128_f8f6f4 v[94:97], v[26:33], v[208:215], v[94:97], v188, v189 op_sel_hi:[0,0,0]
	v_mfma_scale_f32_16x16x128_f8f6f4 v[90:93], v[18:25], v[208:215], v[90:93], v188, v189 op_sel_hi:[0,0,0]
	v_mfma_scale_f32_16x16x128_f8f6f4 v[78:81], v[26:33], v[216:223], v[78:81], v188, v189 op_sel_hi:[0,0,0]
	v_mfma_scale_f32_16x16x128_f8f6f4 v[74:77], v[18:25], v[216:223], v[74:77], v188, v189 op_sel_hi:[0,0,0]
	v_mfma_scale_f32_16x16x128_f8f6f4 v[62:65], v[26:33], v[224:231], v[62:65], v188, v189 op_sel_hi:[0,0,0]
	v_mfma_scale_f32_16x16x128_f8f6f4 v[58:61], v[18:25], v[224:231], v[58:61], v188, v189 op_sel_hi:[0,0,0]
	v_mfma_scale_f32_16x16x128_f8f6f4 v[46:49], v[26:33], v[232:239], v[46:49], v188, v189 op_sel_hi:[0,0,0]
	v_mfma_scale_f32_16x16x128_f8f6f4 v[42:45], v[18:25], v[232:239], v[42:45], v188, v189 op_sel_hi:[0,0,0]
	s_setprio 0
	s_setprio 1
	v_mfma_scale_f32_16x16x128_f8f6f4 v[86:89], v[10:17], v[208:215], v[86:89], v188, v189 op_sel_hi:[0,0,0]
	v_mfma_scale_f32_16x16x128_f8f6f4 v[82:85], v[2:9], v[208:215], v[82:85], v188, v189 op_sel_hi:[0,0,0]
	v_mfma_scale_f32_16x16x128_f8f6f4 v[70:73], v[10:17], v[216:223], v[70:73], v188, v189 op_sel_hi:[0,0,0]
	v_mfma_scale_f32_16x16x128_f8f6f4 v[66:69], v[2:9], v[216:223], v[66:69], v188, v189 op_sel_hi:[0,0,0]
	v_mfma_scale_f32_16x16x128_f8f6f4 v[54:57], v[10:17], v[224:231], v[54:57], v188, v189 op_sel_hi:[0,0,0]
	v_mfma_scale_f32_16x16x128_f8f6f4 v[50:53], v[2:9], v[224:231], v[50:53], v188, v189 op_sel_hi:[0,0,0]
	v_mfma_scale_f32_16x16x128_f8f6f4 v[38:41], v[10:17], v[232:239], v[38:41], v188, v189 op_sel_hi:[0,0,0]
	v_mfma_scale_f32_16x16x128_f8f6f4 v[34:37], v[2:9], v[232:239], v[34:37], v188, v189 op_sel_hi:[0,0,0]
	s_setprio 0
	s_barrier
	s_add_u32 s34, s34, 0x100
	s_addc_u32 s35, s35, 0
	s_add_u32 s36, s36, 0x100
	s_addc_u32 s37, s37, 0
	s_cmp_ge_i32 s23, s49
	s_cbranch_scc1 .LBB0_1444
	s_branch .LBB0_1443
